# bundle1 + P6 router/top-k: 36 ds_bpermute butterfly hops replaced by DPP row ops (quad_perm/row_mirror/row_bcast + readlane broadcast), same association order
# speedup vs baseline: 1.0120x; 1.0009x over previous
; #define LAS __attribute__((address_space(3)))
; __device__ __forceinline__ unsigned pk2(float lo, float hi) { unsigned r; asm volatile("v_cvt_pk_bf16_f32 %0, %1, %2" : "=v"(r) : "v"(lo), "v"(hi)); return r; }
; __device__ __forceinline__ float bflo(unsigned w) { return __uint_as_float(w << 16); }
; __device__ __forceinline__ float bfhi(unsigned w) { return __uint_as_float(w & 0xffff0000u); }
; __device__ __forceinline__ unsigned pk4_fp8(float a, float b, float c, float d) { int w = 0; w = __builtin_amdgcn_cvt_pk_fp8_f32(clamp448(a), clamp448(b), w, false); w = __builtin_amdgcn_cvt_pk_fp8_f32(clamp448(c), clamp448(d), w, true); return (unsigned)w; }
; template <bool DRY> __device__ __forceinline__ void p6_item(Ctx& F, int item) {
;     ...
;         for (int i = 0; i < 2; ++i) { const int rl = 2 * w + i, t = t0 + 16 * ps + rl;
;             f32x4 v[4][2]; float ss = 0.f;
; #pragma unroll
;             for (int j = 0; j < 4; ++j) { const u32x4 xw = xq[i][j]; v[j][0] = (f32x4){bflo(xw.x), bfhi(xw.x), bflo(xw.y), bfhi(xw.y)}; v[j][1] = (f32x4){bflo(xw.z), bfhi(xw.z), bflo(xw.w), bfhi(xw.w)};
; #pragma unroll
;                 for (int h = 0; h < 2; ++h) ss += (v[j][h].x * v[j][h].x + v[j][h].y * v[j][h].y) + (v[j][h].z * v[j][h].z + v[j][h].w * v[j][h].w); }
;             const float rstd = rsqrtf(wave_sum(ss) * (1.0f / DM) + EPS);
; #pragma unroll
;             for (int j = 0; j < 4; ++j) { const int c = 8 * lane + 512 * j; const f32x4 o0 = v[j][0] * rstd * *(const LAS f32x4*)(ggL + c) + *(const LAS f32x4*)(shL + c), o1 = v[j][1] * rstd * *(const LAS f32x4*)(ggL + c + 4) + *(const LAS f32x4*)(shL + c + 4);
;                 u32x4 wv; wv.x = pk2(o0.x, o0.y); wv.y = pk2(o0.z, o0.w); wv.z = pk2(o1.x, o1.y); wv.w = pk2(o1.z, o1.w);
;                 *(LAS u32x4*)(hA + rl * HAP + 8 * lane + 512 * j) = wv;
;                 u32x2 w8; w8.x = pk4_fp8(o0.x * SC_H8, o0.y * SC_H8, o0.z * SC_H8, o0.w * SC_H8); w8.y = pk4_fp8(o1.x * SC_H8, o1.y * SC_H8, o1.z * SC_H8, o1.w * SC_H8);
;                 *(u32x2*)(h8 + (size_t)t * DM + 8 * lane + 512 * j) = w8; }
.LBB0_585:
	s_waitcnt vmcnt(7)
	v_and_b32_e32 v227, 0xffff0000, v36
	v_and_b32_e32 v226, 0xffff0000, v34
	v_and_b32_e32 v233, 0xffff0000, v37
	v_and_b32_e32 v232, 0xffff0000, v35
	v_lshlrev_b32_e32 v189, 16, v36
	v_lshlrev_b32_e32 v188, 16, v34
	v_lshlrev_b32_e32 v229, 16, v37
	v_lshlrev_b32_e32 v228, 16, v35
	v_pk_mul_f32 v[154:155], v[226:227], v[226:227]
	s_waitcnt lgkmcnt(0)
	v_pk_mul_f32 v[156:157], v[232:233], v[232:233]
	v_pk_fma_f32 v[154:155], v[188:189], v[188:189], v[154:155]
	v_pk_fma_f32 v[156:157], v[228:229], v[228:229], v[156:157]
	s_waitcnt vmcnt(6)
	v_and_b32_e32 v179, 0xffff0000, v39
	v_and_b32_e32 v178, 0xffff0000, v38
	v_pk_add_f32 v[154:155], v[154:155], v[156:157]
	v_lshlrev_b32_e32 v172, 16, v40
	v_and_b32_e32 v173, 0xffff0000, v40
	v_lshlrev_b32_e32 v177, 16, v39
	v_lshlrev_b32_e32 v176, 16, v38
	v_pk_mul_f32 v[156:157], v[178:179], v[178:179]
	v_lshlrev_b32_e32 v174, 16, v41
	s_waitcnt vmcnt(5)
	v_lshlrev_b32_e32 v168, 16, v42
	v_pk_fma_f32 v[156:157], v[176:177], v[176:177], v[156:157]
	v_mul_f32_e32 v169, v172, v172
	v_mul_f32_e32 v159, v173, v173
	v_and_b32_e32 v175, 0xffff0000, v41
	v_mul_f32_e32 v114, v174, v174
	v_mov_b32_e32 v158, v168
	v_pk_add_f32 v[154:155], v[154:155], v[154:155] op_sel_hi:[0,1]
	v_pk_add_f32 v[156:157], v[156:157], v[156:157] op_sel_hi:[0,1]
	v_pk_fma_f32 v[160:161], v[174:175], v[174:175], v[114:115] op_sel_hi:[1,1,0]
	v_and_b32_e32 v238, 0xffff0000, v42
	v_lshlrev_b32_e32 v170, 16, v43
	v_and_b32_e32 v171, 0xffff0000, v43
	v_pk_add_f32 v[158:159], v[168:169], v[158:159]
	v_mul_f32_e32 v160, v238, v238
	v_mul_f32_e32 v154, v170, v170
	v_mul_f32_e32 v156, v171, v171
	v_mul_f32_e32 v162, v168, v168
	v_mov_b32_e32 v163, v159
	v_pk_add_f32 v[158:159], v[162:163], v[160:161]
	v_pk_add_f32 v[154:155], v[154:155], v[156:157]
	v_and_b32_e32 v165, 0xffff0000, v45
	v_pk_add_f32 v[154:155], v[158:159], v[154:155]
	v_and_b32_e32 v164, 0xffff0000, v44
	v_pk_add_f32 v[158:159], v[154:155], v[154:155] op_sel_hi:[0,1]
	v_lshlrev_b32_e32 v167, 16, v45
	v_lshlrev_b32_e32 v166, 16, v44
	v_pk_mul_f32 v[154:155], v[164:165], v[164:165]
	s_waitcnt vmcnt(4)
	v_lshlrev_b32_e32 v160, 16, v46
	v_and_b32_e32 v161, 0xffff0000, v46
	v_lshlrev_b32_e32 v156, 16, v48
	v_lshlrev_b32_e32 v162, 16, v47
	v_pk_fma_f32 v[154:155], v[166:167], v[166:167], v[154:155]
	v_mul_f32_e32 v157, v160, v160
	v_mul_f32_e32 v183, v161, v161
	v_and_b32_e32 v163, 0xffff0000, v47
	v_mul_f32_e32 v114, v162, v162
	v_mov_b32_e32 v182, v156
	v_pk_add_f32 v[180:181], v[154:155], v[154:155] op_sel_hi:[0,1]
	v_and_b32_e32 v149, 0xffff0000, v48
	v_lshlrev_b32_e32 v154, 16, v49
	v_and_b32_e32 v155, 0xffff0000, v49
	v_pk_fma_f32 v[184:185], v[162:163], v[162:163], v[114:115] op_sel_hi:[1,1,0]
	v_pk_add_f32 v[182:183], v[156:157], v[182:183]
	v_mul_f32_e32 v184, v149, v149
	v_mul_f32_e32 v180, v154, v154
	v_mul_f32_e32 v158, v155, v155
	v_mul_f32_e32 v186, v156, v156
	v_mov_b32_e32 v187, v183
	v_pk_add_f32 v[182:183], v[186:187], v[184:185]
	v_pk_add_f32 v[158:159], v[180:181], v[158:159]
	s_mov_b32 s3, 0x800000
	v_pk_add_f32 v[158:159], v[182:183], v[158:159]
	v_mov_b32_e32 v180, v188
	v_add_f32_e32 v114, v158, v159
	v_mov_b32_e32 v181, v226
	s_sub_i32 s0, s66, 17
	s_ashr_i32 s1, s0, 31
	s_lshl_b64 s[0:1], s[0:1], 11
	s_waitcnt lgkmcnt(0)
	s_nop 1
	v_add_f32_dpp v114, v114, v114 quad_perm:[1,0,3,2] row_mask:0xf bank_mask:0xf
	v_mov_b32_e32 v226, v189
	v_lshl_add_u64 v[158:159], v[144:145], 0, s[0:1]
	s_mul_i32 s0, s67, 0x2020
	s_waitcnt lgkmcnt(0)
	s_nop 1
	v_add_f32_dpp v114, v114, v114 quad_perm:[2,3,0,1] row_mask:0xf bank_mask:0xf
	s_waitcnt lgkmcnt(0)
	s_nop 1
	v_add_f32_dpp v114, v114, v114 row_half_mirror row_mask:0xf bank_mask:0xf
	s_waitcnt lgkmcnt(0)
	s_nop 1
	v_add_f32_dpp v114, v114, v114 row_mirror row_mask:0xf bank_mask:0xf
	s_waitcnt lgkmcnt(0)
	s_nop 1
	v_add_f32_dpp v114, v114, v114 row_bcast:15 row_mask:0xa bank_mask:0xf
	s_waitcnt lgkmcnt(0)
	s_nop 1
	v_add_f32_dpp v114, v114, v114 row_bcast:31 row_mask:0xc bank_mask:0xf
	s_nop 1
	v_readlane_b32 s98, v114, 63
	s_nop 1
	v_mov_b32_e32 v114, s98
	v_fmamk_f32 v114, v114, 0x3a000000, v210
	v_cmp_gt_f32_e32 vcc, s3, v114
	v_mul_f32_e32 v157, 0x4b800000, v114
	s_nop 0
	v_cndmask_b32_e32 v114, v114, v157, vcc
	v_rsq_f32_e32 v114, v114
	s_nop 0
	v_mul_f32_e32 v157, 0x45800000, v114
	v_cndmask_b32_e32 v114, v114, v157, vcc
	v_pk_mul_f32 v[234:235], v[114:115], v[180:181] op_sel_hi:[0,1]
	v_mov_b32_e32 v180, v228
	v_mov_b32_e32 v181, v232
	v_pk_mul_f32 v[236:237], v[114:115], v[180:181] op_sel_hi:[0,1]
	ds_read_b128 v[180:183], v198
	ds_read_b128 v[184:187], v198 offset:16
	ds_read_b128 v[218:221], v199
	ds_read_b128 v[222:225], v199 offset:16
	v_mov_b32_e32 v232, v229
	v_pk_mul_f32 v[172:173], v[114:115], v[172:173] op_sel_hi:[0,1]
	v_pk_mul_f32 v[174:175], v[114:115], v[174:175] op_sel_hi:[0,1]
	s_waitcnt lgkmcnt(1)
	v_pk_fma_f32 v[220:221], v[182:183], v[236:237], v[220:221]
	v_pk_fma_f32 v[218:219], v[180:181], v[234:235], v[218:219]
	v_pk_mul_f32 v[180:181], v[114:115], v[226:227] op_sel_hi:[0,1]
	v_pk_mul_f32 v[182:183], v[114:115], v[232:233] op_sel_hi:[0,1]
	s_waitcnt lgkmcnt(0)
; #define LAS __attribute__((address_space(3)))
; __device__ __forceinline__ unsigned pk2(float lo, float hi) { unsigned r; asm volatile("v_cvt_pk_bf16_f32 %0, %1, %2" : "=v"(r) : "v"(lo), "v"(hi)); return r; }
; __device__ __forceinline__ unsigned pk4_fp8(float a, float b, float c, float d) { int w = 0; w = __builtin_amdgcn_cvt_pk_fp8_f32(clamp448(a), clamp448(b), w, false); w = __builtin_amdgcn_cvt_pk_fp8_f32(clamp448(c), clamp448(d), w, true); return (unsigned)w; }
; template <bool DRY> __device__ __forceinline__ void p6_item(Ctx& F, int item) {
;     ...
; #pragma unroll
;             for (int j = 0; j < 4; ++j) { const int c = 8 * lane + 512 * j; const f32x4 o0 = v[j][0] * rstd * *(const LAS f32x4*)(ggL + c) + *(const LAS f32x4*)(shL + c), o1 = v[j][1] * rstd * *(const LAS f32x4*)(ggL + c + 4) + *(const LAS f32x4*)(shL + c + 4);
;                 u32x4 wv; wv.x = pk2(o0.x, o0.y); wv.y = pk2(o0.z, o0.w); wv.z = pk2(o1.x, o1.y); wv.w = pk2(o1.z, o1.w);
;                 *(LAS u32x4*)(hA + rl * HAP + 8 * lane + 512 * j) = wv;
;                 u32x2 w8; w8.x = pk4_fp8(o0.x * SC_H8, o0.y * SC_H8, o0.z * SC_H8, o0.w * SC_H8); w8.y = pk4_fp8(o1.x * SC_H8, o1.y * SC_H8, o1.z * SC_H8, o1.w * SC_H8);
;                 *(u32x2*)(h8 + (size_t)t * DM + 8 * lane + 512 * j) = w8; }
	v_pk_fma_f32 v[186:187], v[186:187], v[182:183], v[224:225]
	v_pk_fma_f32 v[184:185], v[184:185], v[180:181], v[222:223]
	v_cvt_pk_bf16_f32 v180, v218, v219
	v_add_u32_e32 v224, s0, v196
	v_mul_f32_e32 v157, 0x41800000, v218
	v_mul_f32_e32 v169, 0x41800000, v219
	v_cvt_pk_bf16_f32 v181, v220, v221
	v_cvt_pk_bf16_f32 v182, v184, v185
	v_cvt_pk_bf16_f32 v183, v186, v187
	ds_write_b128 v224, v[180:183]
	v_med3_f32 v157, v157, s33, v213
	v_med3_f32 v169, v169, s33, v213
	v_mov_b32_e32 v180, 0
	v_cvt_pk_fp8_f32 v180, v157, v169
	v_mul_f32_e32 v181, 0x41800000, v220
	v_mul_f32_e32 v182, 0x41800000, v221
	v_med3_f32 v157, v181, s33, v213
	v_med3_f32 v169, v182, s33, v213
	v_cvt_pk_fp8_f32 v180, v157, v169 op_sel:[0,0,1]
	v_mul_f32_e32 v157, 0x41800000, v184
	v_mul_f32_e32 v169, 0x41800000, v185
	v_med3_f32 v157, v157, s33, v213
	v_med3_f32 v169, v169, s33, v213
	v_mov_b32_e32 v181, 0
	v_cvt_pk_fp8_f32 v181, v157, v169
	v_mul_f32_e32 v182, 0x41800000, v186
	v_mul_f32_e32 v183, 0x41800000, v187
	v_med3_f32 v157, v182, s33, v213
	v_med3_f32 v169, v183, s33, v213
	v_cvt_pk_fp8_f32 v181, v157, v169 op_sel:[0,0,1]
	v_pk_mul_f32 v[154:155], v[114:115], v[154:155] op_sel_hi:[0,1]
	s_add_i32 s0, s66, -16
	s_ashr_i32 s1, s0, 31
	global_store_dwordx2 v[158:159], v[180:181], off
	v_mov_b32_e32 v180, v176
	v_mov_b32_e32 v181, v178
	v_mov_b32_e32 v178, v177
	v_pk_mul_f32 v[188:189], v[114:115], v[180:181] op_sel_hi:[0,1]
	v_pk_mul_f32 v[222:223], v[114:115], v[178:179] op_sel_hi:[0,1]
	ds_read_b128 v[176:179], v200
	ds_read_b128 v[180:183], v200 offset:16
	ds_read_b128 v[184:187], v201
	ds_read_b128 v[218:221], v201 offset:16
	s_lshl_b64 s[0:1], s[0:1], 11
	s_waitcnt lgkmcnt(1)
	v_pk_fma_f32 v[176:177], v[188:189], v[176:177], v[184:185]
	s_waitcnt lgkmcnt(0)
	v_pk_fma_f32 v[180:181], v[172:173], v[180:181], v[218:219]
	v_cvt_pk_bf16_f32 v172, v176, v177
	v_mul_f32_e32 v157, 0x41800000, v176
	v_mul_f32_e32 v169, 0x41800000, v177
	v_pk_fma_f32 v[178:179], v[222:223], v[178:179], v[186:187]
	v_pk_fma_f32 v[182:183], v[174:175], v[182:183], v[220:221]
	v_cvt_pk_bf16_f32 v173, v178, v179
	v_cvt_pk_bf16_f32 v174, v180, v181
	v_med3_f32 v157, v157, s33, v213
	v_cvt_pk_bf16_f32 v175, v182, v183
	ds_write_b128 v224, v[172:175] offset:1024
	v_med3_f32 v169, v169, s33, v213
	v_mov_b32_e32 v172, 0
	v_cvt_pk_fp8_f32 v172, v157, v169
	v_mul_f32_e32 v173, 0x41800000, v178
	v_mul_f32_e32 v174, 0x41800000, v179
	v_med3_f32 v157, v173, s33, v213
	v_med3_f32 v169, v174, s33, v213
	v_cvt_pk_fp8_f32 v172, v157, v169 op_sel:[0,0,1]
	v_mul_f32_e32 v157, 0x41800000, v180
	v_mul_f32_e32 v169, 0x41800000, v181
	v_med3_f32 v157, v157, s33, v213
	v_med3_f32 v169, v169, s33, v213
	v_mov_b32_e32 v173, 0
	v_cvt_pk_fp8_f32 v173, v157, v169
	v_mul_f32_e32 v174, 0x41800000, v182
	v_mul_f32_e32 v175, 0x41800000, v183
	v_med3_f32 v157, v174, s33, v213
	v_med3_f32 v169, v175, s33, v213
	v_cvt_pk_fp8_f32 v173, v157, v169 op_sel:[0,0,1]
	v_mov_b32_e32 v169, v238
	v_pk_mul_f32 v[184:185], v[114:115], v[168:169] op_sel_hi:[0,1]
	v_pk_mul_f32 v[186:187], v[114:115], v[170:171] op_sel_hi:[0,1]
	global_store_dwordx2 v[158:159], v[172:173], off offset:512
	ds_read_b128 v[168:171], v202
	ds_read_b128 v[172:175], v202 offset:16
	ds_read_b128 v[176:179], v203
	ds_read_b128 v[180:183], v203 offset:16
	s_waitcnt vmcnt(3)
	v_and_b32_e32 v238, 0xffff0000, v102
	s_waitcnt lgkmcnt(1)
	v_pk_fma_f32 v[168:169], v[184:185], v[168:169], v[176:177]
	v_mov_b32_e32 v177, v164
	v_mov_b32_e32 v164, v167
	v_mov_b32_e32 v176, v166
	v_pk_mul_f32 v[164:165], v[114:115], v[164:165] op_sel_hi:[0,1]
	v_pk_mul_f32 v[176:177], v[114:115], v[176:177] op_sel_hi:[0,1]
	s_waitcnt lgkmcnt(0)
	v_pk_fma_f32 v[174:175], v[164:165], v[174:175], v[182:183]
	v_cvt_pk_bf16_f32 v164, v168, v169
	v_pk_fma_f32 v[170:171], v[186:187], v[170:171], v[178:179]
	v_pk_fma_f32 v[172:173], v[176:177], v[172:173], v[180:181]
	v_cvt_pk_bf16_f32 v165, v170, v171
	v_mul_f32_e32 v157, 0x41800000, v168
	v_cvt_pk_bf16_f32 v166, v172, v173
	v_cvt_pk_bf16_f32 v167, v174, v175
	ds_write_b128 v224, v[164:167] offset:2048
	v_mul_f32_e32 v164, 0x41800000, v169
	v_med3_f32 v157, v157, s33, v213
	v_med3_f32 v167, v164, s33, v213
	v_mov_b32_e32 v164, 0
	v_cvt_pk_fp8_f32 v164, v157, v167
	v_mul_f32_e32 v165, 0x41800000, v170
	v_mul_f32_e32 v166, 0x41800000, v171
	v_med3_f32 v157, v165, s33, v213
	v_med3_f32 v165, v166, s33, v213
	v_cvt_pk_fp8_f32 v164, v157, v165 op_sel:[0,0,1]
	v_mul_f32_e32 v157, 0x41800000, v172
	v_mul_f32_e32 v165, 0x41800000, v173
	v_med3_f32 v157, v157, s33, v213
	v_med3_f32 v168, v165, s33, v213
	v_mov_b32_e32 v165, 0
	v_cvt_pk_fp8_f32 v165, v157, v168
	v_mul_f32_e32 v166, 0x41800000, v174
	v_mul_f32_e32 v167, 0x41800000, v175
	v_med3_f32 v157, v166, s33, v213
	v_med3_f32 v166, v167, s33, v213
	v_cvt_pk_fp8_f32 v165, v157, v166 op_sel:[0,0,1]
	v_pk_mul_f32 v[176:177], v[114:115], v[160:161] op_sel_hi:[0,1]
	v_pk_mul_f32 v[178:179], v[114:115], v[162:163] op_sel_hi:[0,1]
	v_mov_b32_e32 v157, v149
	global_store_dwordx2 v[158:159], v[164:165], off offset:1024
	ds_read_b128 v[160:163], v204
	ds_read_b128 v[164:167], v204 offset:16
	ds_read_b128 v[168:171], v205
	ds_read_b128 v[172:175], v205 offset:16
	v_pk_mul_f32 v[156:157], v[114:115], v[156:157] op_sel_hi:[0,1]
	v_and_b32_e32 v181, 0xffff0000, v80
	v_and_b32_e32 v180, 0xffff0000, v78
	s_waitcnt lgkmcnt(1)
	v_pk_fma_f32 v[160:161], v[176:177], v[160:161], v[168:169]
	s_waitcnt lgkmcnt(0)
; #define LAS __attribute__((address_space(3)))
; __device__ __forceinline__ unsigned pk2(float lo, float hi) { unsigned r; asm volatile("v_cvt_pk_bf16_f32 %0, %1, %2" : "=v"(r) : "v"(lo), "v"(hi)); return r; }
; __device__ __forceinline__ float bflo(unsigned w) { return __uint_as_float(w << 16); }
; __device__ __forceinline__ float bfhi(unsigned w) { return __uint_as_float(w & 0xffff0000u); }
; __device__ __forceinline__ unsigned pk4_fp8(float a, float b, float c, float d) { int w = 0; w = __builtin_amdgcn_cvt_pk_fp8_f32(clamp448(a), clamp448(b), w, false); w = __builtin_amdgcn_cvt_pk_fp8_f32(clamp448(c), clamp448(d), w, true); return (unsigned)w; }
; template <bool DRY> __device__ __forceinline__ void p6_item(Ctx& F, int item) {
;     ...
;         for (int i = 0; i < 2; ++i) { const int rl = 2 * w + i, t = t0 + 16 * ps + rl;
;             f32x4 v[4][2]; float ss = 0.f;
; #pragma unroll
;             for (int j = 0; j < 4; ++j) { const u32x4 xw = xq[i][j]; v[j][0] = (f32x4){bflo(xw.x), bfhi(xw.x), bflo(xw.y), bfhi(xw.y)}; v[j][1] = (f32x4){bflo(xw.z), bfhi(xw.z), bflo(xw.w), bfhi(xw.w)};
; #pragma unroll
;                 for (int h = 0; h < 2; ++h) ss += (v[j][h].x * v[j][h].x + v[j][h].y * v[j][h].y) + (v[j][h].z * v[j][h].z + v[j][h].w * v[j][h].w); }
;             const float rstd = rsqrtf(wave_sum(ss) * (1.0f / DM) + EPS);
; #pragma unroll
;             for (int j = 0; j < 4; ++j) { const int c = 8 * lane + 512 * j; const f32x4 o0 = v[j][0] * rstd * *(const LAS f32x4*)(ggL + c) + *(const LAS f32x4*)(shL + c), o1 = v[j][1] * rstd * *(const LAS f32x4*)(ggL + c + 4) + *(const LAS f32x4*)(shL + c + 4);
;                 u32x4 wv; wv.x = pk2(o0.x, o0.y); wv.y = pk2(o0.z, o0.w); wv.z = pk2(o1.x, o1.y); wv.w = pk2(o1.z, o1.w);
;                 *(LAS u32x4*)(hA + rl * HAP + 8 * lane + 512 * j) = wv;
;                 u32x2 w8; w8.x = pk4_fp8(o0.x * SC_H8, o0.y * SC_H8, o0.z * SC_H8, o0.w * SC_H8); w8.y = pk4_fp8(o1.x * SC_H8, o1.y * SC_H8, o1.z * SC_H8, o1.w * SC_H8);
;                 *(u32x2*)(h8 + (size_t)t * DM + 8 * lane + 512 * j) = w8; }
	v_pk_fma_f32 v[166:167], v[154:155], v[166:167], v[174:175]
	v_cvt_pk_bf16_f32 v154, v160, v161
	v_mul_f32_e32 v114, 0x41800000, v160
	v_mul_f32_e32 v149, 0x41800000, v161
	v_pk_fma_f32 v[162:163], v[178:179], v[162:163], v[170:171]
	v_pk_fma_f32 v[164:165], v[156:157], v[164:165], v[172:173]
	v_cvt_pk_bf16_f32 v155, v162, v163
	v_med3_f32 v114, v114, s33, v213
	v_cvt_pk_bf16_f32 v156, v164, v165
	v_cvt_pk_bf16_f32 v157, v166, v167
	ds_write_b128 v224, v[154:157] offset:3072
	v_med3_f32 v149, v149, s33, v213
	v_mov_b32_e32 v154, 0
	v_cvt_pk_fp8_f32 v154, v114, v149
	v_mul_f32_e32 v155, 0x41800000, v162
	v_mul_f32_e32 v156, 0x41800000, v163
	v_med3_f32 v114, v155, s33, v213
	v_med3_f32 v149, v156, s33, v213
	v_cvt_pk_fp8_f32 v154, v114, v149 op_sel:[0,0,1]
	v_mul_f32_e32 v114, 0x41800000, v164
	v_mul_f32_e32 v149, 0x41800000, v165
	v_med3_f32 v114, v114, s33, v213
	v_med3_f32 v149, v149, s33, v213
	v_mov_b32_e32 v155, 0
	v_cvt_pk_fp8_f32 v155, v114, v149
	v_mul_f32_e32 v156, 0x41800000, v166
	v_mul_f32_e32 v157, 0x41800000, v167
	v_med3_f32 v114, v156, s33, v213
	v_med3_f32 v149, v157, s33, v213
	v_cvt_pk_fp8_f32 v155, v114, v149 op_sel:[0,0,1]
	v_and_b32_e32 v185, 0xffff0000, v81
	v_and_b32_e32 v184, 0xffff0000, v79
	v_lshlrev_b32_e32 v183, 16, v80
	global_store_dwordx2 v[158:159], v[154:155], off offset:1536
	v_lshlrev_b32_e32 v182, 16, v78
	v_lshlrev_b32_e32 v187, 16, v81
	v_lshlrev_b32_e32 v186, 16, v79
	v_pk_mul_f32 v[154:155], v[180:181], v[180:181]
	v_pk_mul_f32 v[156:157], v[184:185], v[184:185]
	v_pk_fma_f32 v[154:155], v[182:183], v[182:183], v[154:155]
	v_pk_fma_f32 v[156:157], v[186:187], v[186:187], v[156:157]
	v_and_b32_e32 v179, 0xffff0000, v91
	v_and_b32_e32 v178, 0xffff0000, v90
	v_pk_add_f32 v[154:155], v[154:155], v[156:157]
	v_lshlrev_b32_e32 v172, 16, v92
	v_and_b32_e32 v173, 0xffff0000, v92
	v_lshlrev_b32_e32 v177, 16, v91
	v_lshlrev_b32_e32 v176, 16, v90
	v_pk_mul_f32 v[156:157], v[178:179], v[178:179]
	v_lshlrev_b32_e32 v174, 16, v93
	v_lshlrev_b32_e32 v168, 16, v102
	v_pk_fma_f32 v[156:157], v[176:177], v[176:177], v[156:157]
	v_mul_f32_e32 v169, v172, v172
	v_mul_f32_e32 v159, v173, v173
	v_and_b32_e32 v175, 0xffff0000, v93
	v_mul_f32_e32 v114, v174, v174
	v_mov_b32_e32 v158, v168
	v_pk_add_f32 v[154:155], v[154:155], v[154:155] op_sel_hi:[0,1]
	v_pk_add_f32 v[156:157], v[156:157], v[156:157] op_sel_hi:[0,1]
	v_pk_fma_f32 v[160:161], v[174:175], v[174:175], v[114:115] op_sel_hi:[1,1,0]
	v_lshlrev_b32_e32 v170, 16, v103
	v_and_b32_e32 v171, 0xffff0000, v103
	v_pk_add_f32 v[158:159], v[168:169], v[158:159]
	v_mul_f32_e32 v160, v238, v238
	v_mul_f32_e32 v154, v170, v170
	v_mul_f32_e32 v156, v171, v171
	v_mul_f32_e32 v162, v168, v168
	v_mov_b32_e32 v163, v159
	v_pk_add_f32 v[158:159], v[162:163], v[160:161]
	v_pk_add_f32 v[154:155], v[154:155], v[156:157]
	v_and_b32_e32 v165, 0xffff0000, v105
	v_pk_add_f32 v[154:155], v[158:159], v[154:155]
	v_and_b32_e32 v164, 0xffff0000, v104
	v_pk_add_f32 v[162:163], v[154:155], v[154:155] op_sel_hi:[0,1]
	v_lshlrev_b32_e32 v167, 16, v105
	v_lshlrev_b32_e32 v166, 16, v104
	v_pk_mul_f32 v[154:155], v[164:165], v[164:165]
	s_waitcnt vmcnt(4)
	v_lshlrev_b32_e32 v158, 16, v110
	v_and_b32_e32 v159, 0xffff0000, v110
	v_lshlrev_b32_e32 v156, 16, v112
	v_lshlrev_b32_e32 v160, 16, v111
	v_pk_fma_f32 v[154:155], v[166:167], v[166:167], v[154:155]
	v_mul_f32_e32 v157, v158, v158
	v_mul_f32_e32 v219, v159, v159
	v_and_b32_e32 v161, 0xffff0000, v111
	v_mul_f32_e32 v114, v160, v160
	v_mov_b32_e32 v218, v156
	v_pk_add_f32 v[188:189], v[154:155], v[154:155] op_sel_hi:[0,1]
	v_and_b32_e32 v149, 0xffff0000, v112
	v_lshlrev_b32_e32 v154, 16, v113
	v_and_b32_e32 v155, 0xffff0000, v113
	v_pk_fma_f32 v[220:221], v[160:161], v[160:161], v[114:115] op_sel_hi:[1,1,0]
	v_pk_add_f32 v[218:219], v[156:157], v[218:219]
	v_mul_f32_e32 v220, v149, v149
	v_mul_f32_e32 v188, v154, v154
	v_mul_f32_e32 v162, v155, v155
	v_mul_f32_e32 v222, v156, v156
	v_mov_b32_e32 v223, v219
	v_pk_add_f32 v[218:219], v[222:223], v[220:221]
	v_pk_add_f32 v[162:163], v[188:189], v[162:163]
	v_mov_b32_e32 v188, v182
	v_pk_add_f32 v[162:163], v[218:219], v[162:163]
	v_mov_b32_e32 v218, v186
	v_add_f32_e32 v114, v162, v163
	v_mov_b32_e32 v219, v184
	v_mov_b32_e32 v189, v180
	v_mov_b32_e32 v180, v183
	v_mov_b32_e32 v184, v187
	s_waitcnt lgkmcnt(0)
	s_nop 1
	v_add_f32_dpp v114, v114, v114 quad_perm:[1,0,3,2] row_mask:0xf bank_mask:0xf
	v_lshl_add_u64 v[162:163], v[144:145], 0, s[0:1]
	s_waitcnt lgkmcnt(0)
	s_nop 1
	v_add_f32_dpp v114, v114, v114 quad_perm:[2,3,0,1] row_mask:0xf bank_mask:0xf
	s_waitcnt lgkmcnt(0)
	s_nop 1
	v_add_f32_dpp v114, v114, v114 row_half_mirror row_mask:0xf bank_mask:0xf
	s_waitcnt lgkmcnt(0)
	s_nop 1
	v_add_f32_dpp v114, v114, v114 row_mirror row_mask:0xf bank_mask:0xf
	s_waitcnt lgkmcnt(0)
	s_nop 1
	v_add_f32_dpp v114, v114, v114 row_bcast:15 row_mask:0xa bank_mask:0xf
	s_waitcnt lgkmcnt(0)
	s_nop 1
	v_add_f32_dpp v114, v114, v114 row_bcast:31 row_mask:0xc bank_mask:0xf
	s_nop 1
	v_readlane_b32 s98, v114, 63
	s_nop 1
	v_mov_b32_e32 v114, s98
	v_fmamk_f32 v114, v114, 0x3a000000, v210
	v_cmp_gt_f32_e32 vcc, s3, v114
	v_mul_f32_e32 v157, 0x4b800000, v114
	s_nop 0
	v_cndmask_b32_e32 v114, v114, v157, vcc
	v_rsq_f32_e32 v114, v114
	s_nop 0
	v_mul_f32_e32 v157, 0x45800000, v114
	v_cndmask_b32_e32 v114, v114, v157, vcc
	v_pk_mul_f32 v[236:237], v[114:115], v[218:219] op_sel_hi:[0,1]
	ds_read_b128 v[218:221], v198
	ds_read_b128 v[222:225], v198 offset:16
	ds_read_b128 v[226:229], v199
	ds_read_b128 v[232:235], v199 offset:16
	v_pk_mul_f32 v[188:189], v[114:115], v[188:189] op_sel_hi:[0,1]
	v_pk_mul_f32 v[180:181], v[114:115], v[180:181] op_sel_hi:[0,1]
	v_pk_mul_f32 v[182:183], v[114:115], v[184:185] op_sel_hi:[0,1]
	s_waitcnt lgkmcnt(1)
; #define LAS __attribute__((address_space(3)))
; __device__ __forceinline__ unsigned pk2(float lo, float hi) { unsigned r; asm volatile("v_cvt_pk_bf16_f32 %0, %1, %2" : "=v"(r) : "v"(lo), "v"(hi)); return r; }
; __device__ __forceinline__ unsigned pk4_fp8(float a, float b, float c, float d) { int w = 0; w = __builtin_amdgcn_cvt_pk_fp8_f32(clamp448(a), clamp448(b), w, false); w = __builtin_amdgcn_cvt_pk_fp8_f32(clamp448(c), clamp448(d), w, true); return (unsigned)w; }
; template <bool DRY> __device__ __forceinline__ void p6_item(Ctx& F, int item) {
;     ...
; #pragma unroll
;             for (int j = 0; j < 4; ++j) { const int c = 8 * lane + 512 * j; const f32x4 o0 = v[j][0] * rstd * *(const LAS f32x4*)(ggL + c) + *(const LAS f32x4*)(shL + c), o1 = v[j][1] * rstd * *(const LAS f32x4*)(ggL + c + 4) + *(const LAS f32x4*)(shL + c + 4);
;                 u32x4 wv; wv.x = pk2(o0.x, o0.y); wv.y = pk2(o0.z, o0.w); wv.z = pk2(o1.x, o1.y); wv.w = pk2(o1.z, o1.w);
;                 *(LAS u32x4*)(hA + rl * HAP + 8 * lane + 512 * j) = wv;
;                 u32x2 w8; w8.x = pk4_fp8(o0.x * SC_H8, o0.y * SC_H8, o0.z * SC_H8, o0.w * SC_H8); w8.y = pk4_fp8(o1.x * SC_H8, o1.y * SC_H8, o1.z * SC_H8, o1.w * SC_H8);
;                 *(u32x2*)(h8 + (size_t)t * DM + 8 * lane + 512 * j) = w8; }
	v_pk_fma_f32 v[188:189], v[218:219], v[188:189], v[226:227]
	s_waitcnt lgkmcnt(0)
	v_pk_fma_f32 v[184:185], v[224:225], v[182:183], v[234:235]
	v_pk_fma_f32 v[186:187], v[222:223], v[180:181], v[232:233]
	v_cvt_pk_bf16_f32 v180, v188, v189
	v_add_u32_e32 v224, s75, v196
	v_mul_f32_e32 v157, 0x41800000, v188
	v_mul_f32_e32 v169, 0x41800000, v189
	v_pk_fma_f32 v[220:221], v[220:221], v[236:237], v[228:229]
	v_med3_f32 v157, v157, s33, v213
	v_cvt_pk_bf16_f32 v181, v220, v221
	v_cvt_pk_bf16_f32 v182, v186, v187
	v_cvt_pk_bf16_f32 v183, v184, v185
	ds_write_b128 v224, v[180:183]
	v_med3_f32 v169, v169, s33, v213
	v_mov_b32_e32 v180, 0
	v_cvt_pk_fp8_f32 v180, v157, v169
	v_mul_f32_e32 v181, 0x41800000, v220
	v_mul_f32_e32 v182, 0x41800000, v221
	v_med3_f32 v157, v181, s33, v213
	v_med3_f32 v169, v182, s33, v213
	v_cvt_pk_fp8_f32 v180, v157, v169 op_sel:[0,0,1]
	v_mul_f32_e32 v157, 0x41800000, v186
	v_mul_f32_e32 v169, 0x41800000, v187
	v_med3_f32 v157, v157, s33, v213
	v_med3_f32 v169, v169, s33, v213
	v_mov_b32_e32 v181, 0
	v_cvt_pk_fp8_f32 v181, v157, v169
	v_mul_f32_e32 v182, 0x41800000, v184
	v_mul_f32_e32 v183, 0x41800000, v185
	v_med3_f32 v157, v182, s33, v213
	v_med3_f32 v169, v183, s33, v213
	v_cvt_pk_fp8_f32 v181, v157, v169 op_sel:[0,0,1]
	v_pk_mul_f32 v[172:173], v[114:115], v[172:173] op_sel_hi:[0,1]
	v_pk_mul_f32 v[174:175], v[114:115], v[174:175] op_sel_hi:[0,1]
	v_pk_mul_f32 v[154:155], v[114:115], v[154:155] op_sel_hi:[0,1]
	global_store_dwordx2 v[162:163], v[180:181], off
	v_mov_b32_e32 v180, v176
	v_mov_b32_e32 v181, v178
	v_mov_b32_e32 v178, v177
	v_pk_mul_f32 v[188:189], v[114:115], v[180:181] op_sel_hi:[0,1]
	v_pk_mul_f32 v[222:223], v[114:115], v[178:179] op_sel_hi:[0,1]
	ds_read_b128 v[176:179], v200
	ds_read_b128 v[180:183], v200 offset:16
	ds_read_b128 v[184:187], v201
	ds_read_b128 v[218:221], v201 offset:16
	s_waitcnt lgkmcnt(1)
	v_pk_fma_f32 v[176:177], v[188:189], v[176:177], v[184:185]
	s_waitcnt lgkmcnt(0)
	v_pk_fma_f32 v[180:181], v[172:173], v[180:181], v[218:219]
	v_cvt_pk_bf16_f32 v172, v176, v177
	v_mul_f32_e32 v157, 0x41800000, v176
	v_mul_f32_e32 v169, 0x41800000, v177
	v_pk_fma_f32 v[178:179], v[222:223], v[178:179], v[186:187]
	v_pk_fma_f32 v[182:183], v[174:175], v[182:183], v[220:221]
	v_cvt_pk_bf16_f32 v173, v178, v179
	v_cvt_pk_bf16_f32 v174, v180, v181
	v_med3_f32 v157, v157, s33, v213
	v_cvt_pk_bf16_f32 v175, v182, v183
	ds_write_b128 v224, v[172:175] offset:1024
	v_med3_f32 v169, v169, s33, v213
	v_mov_b32_e32 v172, 0
	v_cvt_pk_fp8_f32 v172, v157, v169
	v_mul_f32_e32 v173, 0x41800000, v178
	v_mul_f32_e32 v174, 0x41800000, v179
	v_med3_f32 v157, v173, s33, v213
	v_med3_f32 v169, v174, s33, v213
	v_cvt_pk_fp8_f32 v172, v157, v169 op_sel:[0,0,1]
	v_mul_f32_e32 v157, 0x41800000, v180
	v_mul_f32_e32 v169, 0x41800000, v181
	v_med3_f32 v157, v157, s33, v213
	v_med3_f32 v169, v169, s33, v213
	v_mov_b32_e32 v173, 0
	v_cvt_pk_fp8_f32 v173, v157, v169
	v_mul_f32_e32 v174, 0x41800000, v182
	v_mul_f32_e32 v175, 0x41800000, v183
	v_med3_f32 v157, v174, s33, v213
	v_med3_f32 v169, v175, s33, v213
	v_cvt_pk_fp8_f32 v173, v157, v169 op_sel:[0,0,1]
	v_mov_b32_e32 v169, v238
	v_pk_mul_f32 v[184:185], v[114:115], v[168:169] op_sel_hi:[0,1]
	v_pk_mul_f32 v[186:187], v[114:115], v[170:171] op_sel_hi:[0,1]
	global_store_dwordx2 v[162:163], v[172:173], off offset:512
	ds_read_b128 v[168:171], v202
	ds_read_b128 v[172:175], v202 offset:16
	ds_read_b128 v[176:179], v203
	ds_read_b128 v[180:183], v203 offset:16
	s_waitcnt lgkmcnt(1)
	v_pk_fma_f32 v[168:169], v[184:185], v[168:169], v[176:177]
	v_mov_b32_e32 v177, v164
	v_mov_b32_e32 v164, v167
	v_mov_b32_e32 v176, v166
	v_pk_mul_f32 v[164:165], v[114:115], v[164:165] op_sel_hi:[0,1]
	v_pk_mul_f32 v[176:177], v[114:115], v[176:177] op_sel_hi:[0,1]
	s_waitcnt lgkmcnt(0)
	v_pk_fma_f32 v[174:175], v[164:165], v[174:175], v[182:183]
	v_cvt_pk_bf16_f32 v164, v168, v169
	v_pk_fma_f32 v[170:171], v[186:187], v[170:171], v[178:179]
	v_pk_fma_f32 v[172:173], v[176:177], v[172:173], v[180:181]
	v_cvt_pk_bf16_f32 v165, v170, v171
	v_mul_f32_e32 v157, 0x41800000, v168
	v_cvt_pk_bf16_f32 v166, v172, v173
	v_cvt_pk_bf16_f32 v167, v174, v175
	ds_write_b128 v224, v[164:167] offset:2048
	v_mul_f32_e32 v164, 0x41800000, v169
	v_med3_f32 v157, v157, s33, v213
	v_med3_f32 v167, v164, s33, v213
	v_mov_b32_e32 v164, 0
	v_cvt_pk_fp8_f32 v164, v157, v167
	v_mul_f32_e32 v165, 0x41800000, v170
	v_mul_f32_e32 v166, 0x41800000, v171
	v_med3_f32 v157, v165, s33, v213
	v_med3_f32 v165, v166, s33, v213
	v_cvt_pk_fp8_f32 v164, v157, v165 op_sel:[0,0,1]
	v_mul_f32_e32 v157, 0x41800000, v172
	v_mul_f32_e32 v165, 0x41800000, v173
	v_med3_f32 v157, v157, s33, v213
	v_med3_f32 v168, v165, s33, v213
	v_mov_b32_e32 v165, 0
	v_cvt_pk_fp8_f32 v165, v157, v168
	v_mul_f32_e32 v166, 0x41800000, v174
	v_mul_f32_e32 v167, 0x41800000, v175
	v_med3_f32 v157, v166, s33, v213
	v_med3_f32 v166, v167, s33, v213
	v_cvt_pk_fp8_f32 v165, v157, v166 op_sel:[0,0,1]
	v_pk_mul_f32 v[176:177], v[114:115], v[158:159] op_sel_hi:[0,1]
	v_pk_mul_f32 v[178:179], v[114:115], v[160:161] op_sel_hi:[0,1]
	v_mov_b32_e32 v157, v149
	global_store_dwordx2 v[162:163], v[164:165], off offset:1024
	ds_read_b128 v[158:161], v204
	ds_read_b128 v[164:167], v204 offset:16
	ds_read_b128 v[168:171], v205
	ds_read_b128 v[172:175], v205 offset:16
	v_pk_mul_f32 v[156:157], v[114:115], v[156:157] op_sel_hi:[0,1]
	s_waitcnt lgkmcnt(1)
	v_pk_fma_f32 v[158:159], v[176:177], v[158:159], v[168:169]
	s_waitcnt lgkmcnt(0)
	v_pk_fma_f32 v[166:167], v[154:155], v[166:167], v[174:175]
	v_cvt_pk_bf16_f32 v154, v158, v159
	v_mul_f32_e32 v114, 0x41800000, v158
	v_mul_f32_e32 v149, 0x41800000, v159
	v_pk_fma_f32 v[160:161], v[178:179], v[160:161], v[170:171]
	v_pk_fma_f32 v[164:165], v[156:157], v[164:165], v[172:173]
	v_cvt_pk_bf16_f32 v155, v160, v161
	v_med3_f32 v114, v114, s33, v213
	v_cvt_pk_bf16_f32 v156, v164, v165
	v_cvt_pk_bf16_f32 v157, v166, v167
	ds_write_b128 v224, v[154:157] offset:3072
	v_med3_f32 v149, v149, s33, v213
	v_mov_b32_e32 v154, 0
	v_cvt_pk_fp8_f32 v154, v114, v149
	v_mul_f32_e32 v155, 0x41800000, v160
	v_mul_f32_e32 v156, 0x41800000, v161
	v_med3_f32 v114, v155, s33, v213
	v_med3_f32 v149, v156, s33, v213
	v_cvt_pk_fp8_f32 v154, v114, v149 op_sel:[0,0,1]
	v_mul_f32_e32 v114, 0x41800000, v164
	v_mul_f32_e32 v149, 0x41800000, v165
	v_med3_f32 v114, v114, s33, v213
	v_med3_f32 v149, v149, s33, v213
	v_mov_b32_e32 v155, 0
	v_cvt_pk_fp8_f32 v155, v114, v149
	v_mul_f32_e32 v156, 0x41800000, v166
	v_mul_f32_e32 v157, 0x41800000, v167
	v_med3_f32 v114, v156, s33, v213
	v_med3_f32 v149, v157, s33, v213
	v_cvt_pk_fp8_f32 v155, v114, v149 op_sel:[0,0,1]
	global_store_dwordx2 v[162:163], v[154:155], off offset:1536
	s_waitcnt lgkmcnt(0)
	s_barrier
; #define LAS __attribute__((address_space(3)))
; #define LDS_BARRIER() do { asm volatile("s_waitcnt lgkmcnt(0)" ::: "memory"); __builtin_amdgcn_s_barrier(); asm volatile("" ::: "memory"); } while (0)
; template <bool DRY> __device__ __forceinline__ void p6_item(Ctx& F, int item) {
;     ...
;         {
;             f32x4 acc[4];
; #pragma unroll
;             for (int et = 0; et < 4; ++et) acc[et] = (f32x4){0.f, 0.f, 0.f, 0.f};
; #pragma unroll
;             for (int ks = 3; ks < 6; ++ks)
; #pragma unroll
;                 for (int et = 0; et < 4; ++et) bw2[ks][et] = *(const bf16x8*)(Wr + (size_t)(16 * et + fr) * DM + 256 * w + 64 + 32 * ks + 8 * fq);
;             __builtin_amdgcn_sched_barrier(0);
; #pragma unroll
;             for (int ks = 0; ks < 2; ++ks) { const bf16x8 a = *(const LAS bf16x8*)(hA + fr * HAP + 256 * w + 32 * ks + 8 * fq);
; #pragma unroll
;                 for (int et = 0; et < 4; ++et) acc[et] = __builtin_amdgcn_mfma_f32_16x16x32_bf16(a, bw[ks][et], acc[et], 0, 0, 0); }
; #pragma unroll
;             for (int ks = 0; ks < 6; ++ks) { const bf16x8 a = *(const LAS bf16x8*)(hA + fr * HAP + 256 * w + 64 + 32 * ks + 8 * fq);
; #pragma unroll
;                 for (int et = 0; et < 4; ++et) acc[et] = __builtin_amdgcn_mfma_f32_16x16x32_bf16(a, bw2[ks][et], acc[et], 0, 0, 0); }
; #pragma unroll
;             for (int et = 0; et < 4; ++et)
; #pragma unroll
;                 for (int rr = 0; rr < 4; ++rr) lgt[(w * 16 + 4 * fq + rr) * 65 + 16 * et + fr] = acc[et][rr];
;         }
;         LDS_BARRIER();
;         if (ps + 1 < 4) {
; #pragma unroll
;             for (int i = 0; i < 2; ++i)
; #pragma unroll
;                 for (int j = 0; j < 4; ++j) xq[i][j] = *(const u32x4*)(x1 + (size_t)(t0 + 16 * (ps + 1) + 2 * w + i) * DM + 8 * lane + 512 * j); }
	global_load_dwordx4 v[154:157], v[136:137], off offset:320
	global_load_dwordx4 v[158:161], v[138:139], off offset:320
	global_load_dwordx4 v[162:165], v[140:141], off offset:320
	global_load_dwordx4 v[166:169], v[142:143], off offset:320
	global_load_dwordx4 v[170:173], v[136:137], off offset:384
	global_load_dwordx4 v[174:177], v[138:139], off offset:384
	global_load_dwordx4 v[178:181], v[140:141], off offset:384
	global_load_dwordx4 v[182:185], v[142:143], off offset:384
	global_load_dwordx4 v[218:221], v[136:137], off offset:448
	global_load_dwordx4 v[222:225], v[138:139], off offset:448
	global_load_dwordx4 v[226:229], v[140:141], off offset:448
	global_load_dwordx4 v[232:235], v[142:143], off offset:448
	ds_read_b128 v[236:239], v211
	ds_read_b128 v[186:189], v211 offset:64
	s_cmpk_lg_i32 s74, 0x180
	s_waitcnt lgkmcnt(1)
	v_mfma_f32_16x16x32_bf16 v[240:243], v[236:239], v[10:13], 0
	v_mfma_f32_16x16x32_bf16 v[244:247], v[236:239], v[2:5], 0
	v_mfma_f32_16x16x32_bf16 v[248:251], v[236:239], v[6:9], 0
	v_mfma_f32_16x16x32_bf16 v[236:239], v[236:239], v[18:21], 0
	s_waitcnt lgkmcnt(0)
	v_mfma_f32_16x16x32_bf16 v[240:243], v[186:189], v[14:17], v[240:243]
	v_mfma_f32_16x16x32_bf16 v[244:247], v[186:189], v[22:25], v[244:247]
	v_mfma_f32_16x16x32_bf16 v[248:251], v[186:189], v[26:29], v[248:251]
	v_mfma_f32_16x16x32_bf16 v[186:189], v[186:189], v[30:33], v[236:239]
	s_nop 2
	ds_read_b128 v[236:239], v211 offset:128
	s_waitcnt vmcnt(31) lgkmcnt(0)
	v_mfma_f32_16x16x32_bf16 v[240:243], v[236:239], v[50:53], v[240:243]
	s_waitcnt vmcnt(27)
	v_mfma_f32_16x16x32_bf16 v[244:247], v[236:239], v[66:69], v[244:247]
	v_mfma_f32_16x16x32_bf16 v[248:251], v[236:239], v[58:61], v[248:251]
	s_waitcnt vmcnt(23)
	v_mfma_f32_16x16x32_bf16 v[186:189], v[236:239], v[86:89], v[186:189]
	ds_read_b128 v[236:239], v211 offset:192
	s_waitcnt lgkmcnt(0)
	v_mfma_f32_16x16x32_bf16 v[240:243], v[236:239], v[54:57], v[240:243]
	v_mfma_f32_16x16x32_bf16 v[244:247], v[236:239], v[74:77], v[244:247]
	v_mfma_f32_16x16x32_bf16 v[248:251], v[236:239], v[62:65], v[248:251]
	s_waitcnt vmcnt(21)
	v_mfma_f32_16x16x32_bf16 v[186:189], v[236:239], v[98:101], v[186:189]
	ds_read_b128 v[236:239], v211 offset:256
	s_waitcnt lgkmcnt(0)
	v_mfma_f32_16x16x32_bf16 v[240:243], v[236:239], v[70:73], v[240:243]
	v_mfma_f32_16x16x32_bf16 v[244:247], v[236:239], v[82:85], v[244:247]
	v_mfma_f32_16x16x32_bf16 v[248:251], v[236:239], v[94:97], v[248:251]
	s_waitcnt vmcnt(20)
	v_mfma_f32_16x16x32_bf16 v[186:189], v[236:239], v[106:109], v[186:189]
	ds_read_b128 v[236:239], v211 offset:320
	s_waitcnt vmcnt(8) lgkmcnt(0)
	v_mfma_f32_16x16x32_bf16 v[166:169], v[236:239], v[166:169], v[186:189]
	s_nop 4
	ds_read_b128 v[186:189], v211 offset:384
	v_mfma_f32_16x16x32_bf16 v[154:157], v[236:239], v[154:157], v[240:243]
	s_waitcnt vmcnt(7) lgkmcnt(0)
	v_mfma_f32_16x16x32_bf16 v[154:157], v[186:189], v[170:173], v[154:157]
	ds_read_b128 v[170:173], v211 offset:448
	v_mfma_f32_16x16x32_bf16 v[158:161], v[236:239], v[158:161], v[244:247]
	v_mfma_f32_16x16x32_bf16 v[162:165], v[236:239], v[162:165], v[248:251]
	s_waitcnt vmcnt(6)
	v_mfma_f32_16x16x32_bf16 v[158:161], v[186:189], v[174:177], v[158:161]
	s_waitcnt vmcnt(5)
	v_mfma_f32_16x16x32_bf16 v[162:165], v[186:189], v[178:181], v[162:165]
	s_waitcnt vmcnt(4)
	v_mfma_f32_16x16x32_bf16 v[166:169], v[186:189], v[182:185], v[166:169]
	s_waitcnt vmcnt(3) lgkmcnt(0)
	v_mfma_f32_16x16x32_bf16 v[154:157], v[170:173], v[218:221], v[154:157]
	s_waitcnt vmcnt(2)
	v_mfma_f32_16x16x32_bf16 v[158:161], v[170:173], v[222:225], v[158:161]
	s_waitcnt vmcnt(1)
	v_mfma_f32_16x16x32_bf16 v[162:165], v[170:173], v[226:229], v[162:165]
	s_waitcnt vmcnt(0)
	v_mfma_f32_16x16x32_bf16 v[166:169], v[170:173], v[232:235], v[166:169]
	s_nop 3
	ds_write2_b32 v212, v154, v158 offset1:16
	ds_write2_b32 v212, v155, v159 offset0:65 offset1:81
	ds_write2_b32 v212, v156, v160 offset0:130 offset1:146
	ds_write2_b32 v212, v157, v161 offset0:195 offset1:211
	ds_write2_b32 v212, v162, v166 offset0:32 offset1:48
	ds_write2_b32 v212, v163, v167 offset0:97 offset1:113
	ds_write2_b32 v212, v164, v168 offset0:162 offset1:178
	ds_write2_b32 v212, v165, v169 offset0:227 offset1:243
	s_waitcnt lgkmcnt(0)
	s_barrier
	s_cbranch_scc0 .LBB0_587
	s_add_i32 s0, s66, -1
	s_ashr_i32 s1, s0, 31
	s_lshl_b64 s[0:1], s[0:1], 12
	s_ashr_i32 s67, s66, 31
	v_lshl_add_u64 v[46:47], v[134:135], 0, s[0:1]
	s_lshl_b64 s[0:1], s[66:67], 12
	v_lshl_add_u64 v[110:111], v[134:135], 0, s[0:1]
	global_load_dwordx4 v[34:37], v[46:47], off
	global_load_dwordx4 v[38:41], v[46:47], off offset:1024
	global_load_dwordx4 v[42:45], v[46:47], off offset:2048
	s_nop 0
	global_load_dwordx4 v[46:49], v[46:47], off offset:3072
	s_nop 0
	global_load_dwordx4 v[78:81], v[110:111], off
	global_load_dwordx4 v[90:93], v[110:111], off offset:1024
	global_load_dwordx4 v[102:105], v[110:111], off offset:2048
	s_nop 0
	global_load_dwordx4 v[110:113], v[110:111], off offset:3072
	v_readlane_b32 s67, v253, 57
; __device__ __forceinline__ float sigmoidf_(float x) { return __builtin_amdgcn_rcpf(1.0f + __expf(-x)); }
; template <bool DRY> __device__ __forceinline__ void p6_item(Ctx& F, int item) {
;     ...
;             const int tl = 2 * w + i, tt = 16 * ps + tl; float z = 0.f;
; #pragma unroll
;             for (int w2 = 0; w2 < 8; ++w2) z += lgt[(w2 * 16 + tl) * 65 + lane];
;             const float s = sigmoidf_(z); const float bsc = s + brl;
;             float m1 = bsc; m1 = fmaxf(m1, __shfl_xor(m1, 1)); m1 = fmaxf(m1, __shfl_xor(m1, 2)); m1 = fmaxf(m1, __shfl_xor(m1, 4));
;             const unsigned long long eq = __ballot(bsc == m1); const unsigned gm = (unsigned)(eq >> (8 * g)) & 0xffu;
;             const bool first = (lane & 7) == (__builtin_ctz(gm | 0x100u) & 7);
;             float m2 = first ? -3.0e38f : bsc; m2 = fmaxf(m2, __shfl_xor(m2, 1)); m2 = fmaxf(m2, __shfl_xor(m2, 2)); m2 = fmaxf(m2, __shfl_xor(m2, 4));
;             const float gs = m1 + m2;
;             int rank_g = 0;
; #pragma unroll
;             for (int g2 = 0; g2 < 8; ++g2) { const float o = __int_as_float(__builtin_amdgcn_readlane(__float_as_int(gs), 8 * g2)); rank_g += (o > gs || (o == gs && g2 < g)) ? 1 : 0; }
;             const bool selg = rank_g < 4;
;             unsigned ub = (unsigned)__float_as_int(bsc); ub ^= (ub >> 31) ? 0xffffffffu : 0x80000000u;
.LBB0_587:
	s_mul_i32 s0, s67, 0x208
	v_add_u32_e32 v114, s0, v197
	ds_read_b32 v149, v114
	ds_read_b32 v154, v114 offset:4160
	v_readlane_b32 s22, v254, 26
	v_readlane_b32 s23, v254, 27
	s_waitcnt lgkmcnt(1)
	v_add_f32_e32 v149, 0, v149
	s_waitcnt lgkmcnt(0)
	v_add_f32_e32 v149, v149, v154
	ds_read_b32 v154, v114 offset:8320
	s_waitcnt lgkmcnt(0)
	v_add_f32_e32 v149, v149, v154
	ds_read_b32 v154, v114 offset:12480
	s_waitcnt lgkmcnt(0)
	v_add_f32_e32 v149, v149, v154
	ds_read_b32 v154, v114 offset:16640
	s_waitcnt lgkmcnt(0)
	v_add_f32_e32 v149, v149, v154
	ds_read_b32 v154, v114 offset:20800
	s_waitcnt lgkmcnt(0)
	v_add_f32_e32 v149, v149, v154
	ds_read_b32 v154, v114 offset:24960
	s_waitcnt lgkmcnt(0)
	v_add_f32_e32 v149, v149, v154
	ds_read_b32 v154, v114 offset:29120
	s_waitcnt lgkmcnt(0)
	v_add_f32_e32 v149, v149, v154
	v_mul_f32_e32 v149, 0xbfb8aa3b, v149
	v_exp_f32_e32 v149, v149
	s_nop 0
	v_add_f32_e32 v149, 1.0, v149
	v_rcp_f32_e32 v154, v149
	s_nop 0
	v_add_f32_e32 v149, v153, v154
	s_waitcnt lgkmcnt(0)
	s_nop 1
	v_max_f32_dpp v155, v149, v149 quad_perm:[1,0,3,2] row_mask:0xf bank_mask:0xf
	s_waitcnt lgkmcnt(0)
	s_nop 1
	v_max_f32_dpp v155, v155, v155 quad_perm:[2,3,0,1] row_mask:0xf bank_mask:0xf
	s_waitcnt lgkmcnt(0)
	s_nop 1
	v_max_f32_dpp v155, v155, v155 row_half_mirror row_mask:0xf bank_mask:0xf
	v_cmp_eq_f32_e32 vcc, v149, v155
	s_nop 1
	v_lshrrev_b64 v[156:157], v146, vcc
	v_or_b32_e32 v156, 0x100, v156
	v_ffbl_b32_e32 v156, v156
	v_bitop3_b32 v156, v156, 7, v0 bitop3:0x48
	v_cmp_ne_u32_e32 vcc, 0, v156
	s_nop 1
	v_cndmask_b32_e32 v156, v214, v149, vcc
	s_waitcnt lgkmcnt(0)
	s_nop 1
	v_max_f32_dpp v156, v156, v156 quad_perm:[1,0,3,2] row_mask:0xf bank_mask:0xf
	s_waitcnt lgkmcnt(0)
	s_nop 1
	v_max_f32_dpp v156, v156, v156 quad_perm:[2,3,0,1] row_mask:0xf bank_mask:0xf
	s_waitcnt lgkmcnt(0)
	s_nop 1
	v_max_f32_dpp v156, v156, v156 row_half_mirror row_mask:0xf bank_mask:0xf
	v_add_f32_e32 v155, v155, v156
	s_nop 0
	v_readlane_b32 s0, v155, 0
	s_nop 1
	v_cmp_gt_f32_e32 vcc, s0, v155
	v_cmp_eq_f32_e64 s[0:1], s0, v155
	s_and_b64 s[0:1], s[22:23], s[0:1]
	s_or_b64 s[0:1], vcc, s[0:1]
	v_cndmask_b32_e64 v156, 0, 1, s[0:1]
	v_readlane_b32 s0, v155, 8
	v_readlane_b32 s22, v254, 28
	v_readlane_b32 s23, v254, 29
	v_cmp_gt_f32_e32 vcc, s0, v155
	v_cmp_eq_f32_e64 s[0:1], s0, v155
	s_and_b64 s[0:1], s[22:23], s[0:1]
	s_or_b64 s[0:1], vcc, s[0:1]
	v_cndmask_b32_e64 v157, 0, 1, s[0:1]
	v_readlane_b32 s0, v155, 16
	v_readlane_b32 s22, v254, 32
	v_readlane_b32 s23, v254, 33
	v_cmp_gt_f32_e32 vcc, s0, v155
	v_cmp_eq_f32_e64 s[0:1], s0, v155
	s_and_b64 s[0:1], s[22:23], s[0:1]
	s_or_b64 s[0:1], vcc, s[0:1]
	v_cndmask_b32_e64 v158, 0, 1, s[0:1]
	v_readlane_b32 s0, v155, 24
	v_readlane_b32 s22, v254, 36
	v_readlane_b32 s23, v254, 37
	v_cmp_gt_f32_e32 vcc, s0, v155
	v_cmp_eq_f32_e64 s[0:1], s0, v155
	s_and_b64 s[0:1], s[22:23], s[0:1]
	s_or_b64 s[0:1], vcc, s[0:1]
	v_cndmask_b32_e64 v159, 0, 1, s[0:1]
	v_readlane_b32 s0, v155, 32
	v_readlane_b32 s22, v254, 40
	v_readlane_b32 s23, v254, 41
	v_cmp_gt_f32_e32 vcc, s0, v155
	v_cmp_eq_f32_e64 s[0:1], s0, v155
	s_and_b64 s[0:1], s[22:23], s[0:1]
	s_or_b64 s[0:1], vcc, s[0:1]
	v_cndmask_b32_e64 v160, 0, 1, s[0:1]
	v_readlane_b32 s0, v155, 40
	v_readlane_b32 s22, v254, 44
	v_readlane_b32 s23, v254, 45
	v_cmp_gt_f32_e32 vcc, s0, v155
	v_cmp_eq_f32_e64 s[0:1], s0, v155
	s_and_b64 s[0:1], s[22:23], s[0:1]
	s_or_b64 s[0:1], vcc, s[0:1]
	v_cndmask_b32_e64 v161, 0, 1, s[0:1]
	v_readlane_b32 s0, v155, 48
	v_readlane_b32 s22, v254, 46
	v_readlane_b32 s23, v254, 47
	v_cmp_gt_f32_e32 vcc, s0, v155
	v_cmp_eq_f32_e64 s[0:1], s0, v155
	s_and_b64 s[0:1], s[22:23], s[0:1]
	s_or_b64 s[0:1], vcc, s[0:1]
	v_cndmask_b32_e64 v162, 0, 1, s[0:1]
	v_readlane_b32 s0, v155, 56
	s_nop 1
	v_cmp_gt_f32_e32 vcc, s0, v155
	v_cmp_lt_i32_e64 s[0:1], -1, v149
	s_nop 0
	v_cndmask_b32_e64 v155, 0, 1, vcc
	v_add_u32_e32 v155, v157, v155
	v_add3_u32 v155, v155, v156, v158
	v_add3_u32 v155, v155, v159, v160
	v_add3_u32 v155, v155, v161, v162
	v_cmp_gt_u32_e32 vcc, 4, v155
	v_cndmask_b32_e64 v155, -1, v215, s[0:1]
	s_and_b32 s24, vcc_lo, 1
	v_xor_b32_e32 v149, v155, v149
	v_mov_b32_e32 v155, 0
	s_cmp_eq_u64 s[24:25], 0
	s_cbranch_scc0 .LBB0_609
	s_and_b32 s24, vcc_lo, 0x100
	s_cmp_eq_u64 s[24:25], 0
	s_cbranch_scc0 .LBB0_610

; __device__ __forceinline__ float sigmoidf_(float x) { return __builtin_amdgcn_rcpf(1.0f + __expf(-x)); }
; template <bool DRY> __device__ __forceinline__ void p6_item(Ctx& F, int item) {
;     ...
;             const int tl = 2 * w + i, tt = 16 * ps + tl; float z = 0.f;
; #pragma unroll
;             for (int w2 = 0; w2 < 8; ++w2) z += lgt[(w2 * 16 + tl) * 65 + lane];
;             const float s = sigmoidf_(z); const float bsc = s + brl;
;             float m1 = bsc; m1 = fmaxf(m1, __shfl_xor(m1, 1)); m1 = fmaxf(m1, __shfl_xor(m1, 2)); m1 = fmaxf(m1, __shfl_xor(m1, 4));
;             const unsigned long long eq = __ballot(bsc == m1); const unsigned gm = (unsigned)(eq >> (8 * g)) & 0xffu;
;             const bool first = (lane & 7) == (__builtin_ctz(gm | 0x100u) & 7);
;             float m2 = first ? -3.0e38f : bsc; m2 = fmaxf(m2, __shfl_xor(m2, 1)); m2 = fmaxf(m2, __shfl_xor(m2, 2)); m2 = fmaxf(m2, __shfl_xor(m2, 4));
;             const float gs = m1 + m2;
;             int rank_g = 0;
; #pragma unroll
;             for (int g2 = 0; g2 < 8; ++g2) { const float o = __int_as_float(__builtin_amdgcn_readlane(__float_as_int(gs), 8 * g2)); rank_g += (o > gs || (o == gs && g2 < g)) ? 1 : 0; }
;             const bool selg = rank_g < 4;
;             unsigned ub = (unsigned)__float_as_int(bsc); ub ^= (ub >> 31) ? 0xffffffffu : 0x80000000u;
;     ...
;             const bool chosen = selg && rank < 8;
;             const float wsum = wave_sum(chosen ? s : 0.f);
;             if (chosen) { const int t = t0 + tt; eidx[t * 8 + rank] = lane; wsel[t * 8 + rank] = s * (2.5f / wsum); selE[tt * 8 + rank] = (unsigned char)lane; selL[tt * 8 + rank] = (unsigned char)lc; }
;             lc += chosen ? 1u : 0u;
.LBB0_596:
	v_cmp_gt_u32_e64 s[0:1], 8, v155
	s_and_b64 s[22:23], vcc, s[0:1]
	v_cndmask_b32_e64 v149, 0, v154, s[22:23]
	s_waitcnt lgkmcnt(0)
	s_nop 1
	v_add_f32_dpp v149, v149, v149 quad_perm:[1,0,3,2] row_mask:0xf bank_mask:0xf
	s_waitcnt lgkmcnt(0)
	s_nop 1
	v_add_f32_dpp v149, v149, v149 quad_perm:[2,3,0,1] row_mask:0xf bank_mask:0xf
	s_waitcnt lgkmcnt(0)
	s_nop 1
	v_add_f32_dpp v149, v149, v149 row_half_mirror row_mask:0xf bank_mask:0xf
	s_waitcnt lgkmcnt(0)
	s_nop 1
	v_add_f32_dpp v149, v149, v149 row_mirror row_mask:0xf bank_mask:0xf
	s_waitcnt lgkmcnt(0)
	s_nop 1
	v_add_f32_dpp v149, v149, v149 row_bcast:15 row_mask:0xa bank_mask:0xf
	s_nop 1
	v_add_f32_dpp v149, v149, v149 row_bcast:31 row_mask:0xc bank_mask:0xf
	s_nop 1
	v_readlane_b32 s98, v149, 63
	s_nop 1
	v_mov_b32_e32 v149, s98
	s_and_saveexec_b64 s[0:1], s[22:23]
	s_cbranch_execz .LBB0_598
	v_readlane_b32 s3, v255, 1
	s_add_i32 s3, s74, s3
	s_waitcnt lgkmcnt(0)
	v_add_u32_e32 v156, s3, v155
	s_mov_b32 s3, 0x40200000
	v_div_scale_f32 v160, vcc, v149, v149, s3
	v_rcp_f32_e32 v161, v160
	v_ashrrev_i32_e32 v157, 31, v156
	v_readlane_b32 vcc_lo, v254, 6
	v_lshlrev_b64 v[156:157], 2, v[156:157]
	v_readlane_b32 vcc_hi, v254, 7
	s_nop 1
	v_lshl_add_u64 v[158:159], vcc, 0, v[156:157]
	global_store_dword v[158:159], v230, off
	v_fma_f32 v158, -v160, v161, 1.0
	v_fmac_f32_e32 v161, v158, v161
	v_div_scale_f32 v158, vcc, s3, v149, s3
	v_mul_f32_e32 v159, v158, v161
	v_fma_f32 v162, -v160, v159, v158
	v_fmac_f32_e32 v159, v162, v161
	v_fma_f32 v158, -v160, v159, v158
	v_div_fmas_f32 v158, v158, v161, v159
	v_readlane_b32 vcc_lo, v254, 8
	v_div_fixup_f32 v149, v158, v149, s3
	v_readlane_b32 vcc_hi, v254, 9
	v_readlane_b32 s3, v255, 0
	v_mul_f32_e32 v149, v154, v149
	v_lshl_add_u64 v[156:157], vcc, 0, v[156:157]
	s_add_i32 s3, s74, s3
	global_store_dword v[156:157], v149, off
	v_add_u32_e32 v149, s3, v155
	v_add_u32_e32 v154, 0x18300, v149
	v_add_u32_e32 v149, 0x18500, v149
	ds_write_b8 v154, v230
	ds_write_b8 v149, v216
.LBB0_598:
	s_or_b64 exec, exec, s[0:1]
	v_readlane_b32 s0, v254, 48
	v_readlane_b32 s84, v254, 26
	ds_read_b32 v154, v114 offset:4420
	v_add_u32_e32 v149, s0, v197
	ds_read_b32 v149, v149
	v_readlane_b32 s85, v254, 27
	s_waitcnt lgkmcnt(0)
	v_add_f32_e32 v149, 0, v149
	v_add_f32_e32 v149, v149, v154
	ds_read_b32 v154, v114 offset:8580
	s_waitcnt lgkmcnt(0)
	v_add_f32_e32 v149, v149, v154
	ds_read_b32 v154, v114 offset:12740
	s_waitcnt lgkmcnt(0)
	v_add_f32_e32 v149, v149, v154
	ds_read_b32 v154, v114 offset:16900
	s_waitcnt lgkmcnt(0)
	v_add_f32_e32 v149, v149, v154
	ds_read_b32 v154, v114 offset:21060
	s_waitcnt lgkmcnt(0)
	v_add_f32_e32 v149, v149, v154
	ds_read_b32 v154, v114 offset:25220
	ds_read_b32 v114, v114 offset:29380
	s_waitcnt lgkmcnt(1)
	v_add_f32_e32 v149, v149, v154
	s_waitcnt lgkmcnt(0)
	v_add_f32_e32 v114, v149, v114
	v_mul_f32_e32 v114, 0xbfb8aa3b, v114
	v_exp_f32_e32 v114, v114
	s_nop 0
	v_add_f32_e32 v114, 1.0, v114
	v_rcp_f32_e32 v114, v114
	s_nop 0
	v_add_f32_e32 v149, v153, v114
	s_waitcnt lgkmcnt(0)
	s_nop 1
	v_max_f32_dpp v154, v149, v149 quad_perm:[1,0,3,2] row_mask:0xf bank_mask:0xf
	s_waitcnt lgkmcnt(0)
	s_nop 1
	v_max_f32_dpp v154, v154, v154 quad_perm:[2,3,0,1] row_mask:0xf bank_mask:0xf
	s_waitcnt lgkmcnt(0)
	s_nop 1
	v_max_f32_dpp v156, v154, v154 row_half_mirror row_mask:0xf bank_mask:0xf
	v_cmp_eq_f32_e32 vcc, v149, v156
	s_nop 1
	v_lshrrev_b64 v[154:155], v146, vcc
	v_or_b32_e32 v154, 0x100, v154
	v_ffbl_b32_e32 v154, v154
	v_bitop3_b32 v154, v154, 7, v0 bitop3:0x48
	v_cmp_ne_u32_e32 vcc, 0, v154
	s_nop 1
	v_cndmask_b32_e32 v154, v214, v149, vcc
	s_waitcnt lgkmcnt(0)
	s_nop 1
	v_max_f32_dpp v154, v154, v154 quad_perm:[1,0,3,2] row_mask:0xf bank_mask:0xf
	s_waitcnt lgkmcnt(0)
	s_nop 1
	v_max_f32_dpp v154, v154, v154 quad_perm:[2,3,0,1] row_mask:0xf bank_mask:0xf
	s_waitcnt lgkmcnt(0)
	s_nop 1
	v_max_f32_dpp v154, v154, v154 row_half_mirror row_mask:0xf bank_mask:0xf
	v_add_f32_e32 v154, v156, v154
	s_nop 0
	v_readlane_b32 s0, v154, 0
	s_nop 1
	v_cmp_gt_f32_e32 vcc, s0, v154
	v_cmp_eq_f32_e64 s[0:1], s0, v154
	s_and_b64 s[0:1], s[84:85], s[0:1]
	s_or_b64 s[0:1], vcc, s[0:1]
	v_cndmask_b32_e64 v155, 0, 1, s[0:1]
	v_readlane_b32 s0, v154, 8
	v_readlane_b32 s84, v254, 28
	v_readlane_b32 s85, v254, 29
	v_cmp_gt_f32_e32 vcc, s0, v154
	v_cmp_eq_f32_e64 s[0:1], s0, v154
	s_and_b64 s[0:1], s[84:85], s[0:1]
	s_or_b64 s[0:1], vcc, s[0:1]
	v_cndmask_b32_e64 v156, 0, 1, s[0:1]
	v_readlane_b32 s0, v154, 16
	v_readlane_b32 s84, v254, 32
	v_readlane_b32 s85, v254, 33
	v_cmp_gt_f32_e32 vcc, s0, v154
	v_cmp_eq_f32_e64 s[0:1], s0, v154
	s_and_b64 s[0:1], s[84:85], s[0:1]
	s_or_b64 s[0:1], vcc, s[0:1]
	v_cndmask_b32_e64 v157, 0, 1, s[0:1]
	v_readlane_b32 s0, v154, 24
	v_readlane_b32 s84, v254, 36
	v_readlane_b32 s85, v254, 37
	v_cmp_gt_f32_e32 vcc, s0, v154
	v_cmp_eq_f32_e64 s[0:1], s0, v154
	s_and_b64 s[0:1], s[84:85], s[0:1]
	s_or_b64 s[0:1], vcc, s[0:1]
	v_cndmask_b32_e64 v158, 0, 1, s[0:1]
	v_readlane_b32 s0, v154, 32
	v_readlane_b32 s84, v254, 40
	v_readlane_b32 s85, v254, 41
	v_cmp_gt_f32_e32 vcc, s0, v154
	v_cmp_eq_f32_e64 s[0:1], s0, v154
	s_and_b64 s[0:1], s[84:85], s[0:1]
	s_or_b64 s[0:1], vcc, s[0:1]
	v_cndmask_b32_e64 v159, 0, 1, s[0:1]
	v_readlane_b32 s0, v154, 40
	v_readlane_b32 s84, v254, 44
	v_readlane_b32 s85, v254, 45
	v_cmp_gt_f32_e32 vcc, s0, v154
	v_cmp_eq_f32_e64 s[0:1], s0, v154
	s_and_b64 s[0:1], s[84:85], s[0:1]
	s_or_b64 s[0:1], vcc, s[0:1]
	v_cndmask_b32_e64 v160, 0, 1, s[0:1]
	v_readlane_b32 s0, v154, 48
	v_readlane_b32 s84, v254, 46
	v_readlane_b32 s85, v254, 47
	v_cmp_gt_f32_e32 vcc, s0, v154
	v_cmp_eq_f32_e64 s[0:1], s0, v154
	s_and_b64 s[0:1], s[84:85], s[0:1]
	s_or_b64 s[0:1], vcc, s[0:1]
	v_cndmask_b32_e64 v161, 0, 1, s[0:1]
	v_readlane_b32 s0, v154, 56
	s_nop 1
	v_cmp_gt_f32_e32 vcc, s0, v154
	v_cmp_lt_i32_e64 s[0:1], -1, v149
	s_nop 0
	v_cndmask_b32_e64 v154, 0, 1, vcc
	v_add_u32_e32 v154, v156, v154
	v_add3_u32 v154, v154, v155, v157
	v_add3_u32 v154, v154, v158, v159
	v_add3_u32 v154, v154, v160, v161
	v_cmp_gt_u32_e32 vcc, 4, v154
	v_cndmask_b32_e64 v154, -1, v215, s[0:1]
	s_and_b32 s24, vcc_lo, 1
	v_xor_b32_e32 v149, v154, v149
	v_mov_b32_e32 v154, 0
	s_cmp_eq_u64 s[24:25], 0
	s_cbranch_scc0 .LBB0_616
	s_and_b32 s24, vcc_lo, 0x100
	s_cmp_eq_u64 s[24:25], 0
	s_cbranch_scc0 .LBB0_617

; template <bool DRY> __device__ __forceinline__ void p6_item(Ctx& F, int item) {
;     ...
;             const bool chosen = selg && rank < 8;
;             const float wsum = wave_sum(chosen ? s : 0.f);
;             if (chosen) { const int t = t0 + tt; eidx[t * 8 + rank] = lane; wsel[t * 8 + rank] = s * (2.5f / wsum); selE[tt * 8 + rank] = (unsigned char)lane; selL[tt * 8 + rank] = (unsigned char)lc; }
;             lc += chosen ? 1u : 0u;
.LBB0_607:
	v_cmp_gt_u32_e64 s[0:1], 8, v154
	s_and_b64 s[0:1], vcc, s[0:1]
	v_cndmask_b32_e64 v149, 0, 1, s[22:23]
	v_cndmask_b32_e64 v155, 0, v114, s[0:1]
	v_add_u32_e32 v149, v216, v149
	s_waitcnt lgkmcnt(0)
	s_nop 1
	v_add_f32_dpp v155, v155, v155 quad_perm:[1,0,3,2] row_mask:0xf bank_mask:0xf
	s_waitcnt lgkmcnt(0)
	s_nop 1
	v_add_f32_dpp v155, v155, v155 quad_perm:[2,3,0,1] row_mask:0xf bank_mask:0xf
	s_waitcnt lgkmcnt(0)
	s_nop 1
	v_add_f32_dpp v155, v155, v155 row_half_mirror row_mask:0xf bank_mask:0xf
	s_waitcnt lgkmcnt(0)
	s_nop 1
	v_add_f32_dpp v155, v155, v155 row_mirror row_mask:0xf bank_mask:0xf
	s_waitcnt lgkmcnt(0)
	s_nop 1
	v_add_f32_dpp v155, v155, v155 row_bcast:15 row_mask:0xa bank_mask:0xf
	s_nop 1
	v_add_f32_dpp v155, v155, v155 row_bcast:31 row_mask:0xc bank_mask:0xf
	s_nop 1
	v_readlane_b32 s98, v155, 63
	s_nop 1
	v_mov_b32_e32 v155, s98
	s_and_saveexec_b64 s[22:23], s[0:1]
	s_cbranch_execz .LBB0_584
	v_readlane_b32 s3, v255, 1
	s_add_i32 s3, s74, s3
	s_waitcnt lgkmcnt(0)
	v_add3_u32 v156, s3, v154, 8
	s_mov_b32 s3, 0x40200000
	v_div_scale_f32 v160, vcc, v155, v155, s3
	v_rcp_f32_e32 v161, v160
	v_ashrrev_i32_e32 v157, 31, v156
	v_readlane_b32 vcc_lo, v254, 6
	v_lshlrev_b64 v[156:157], 2, v[156:157]
	v_readlane_b32 vcc_hi, v254, 7
	s_nop 1
	v_lshl_add_u64 v[158:159], vcc, 0, v[156:157]
	global_store_dword v[158:159], v230, off
	v_fma_f32 v158, -v160, v161, 1.0
	v_fmac_f32_e32 v161, v158, v161
	v_div_scale_f32 v158, vcc, s3, v155, s3
	v_mul_f32_e32 v159, v158, v161
	v_fma_f32 v162, -v160, v159, v158
	v_fmac_f32_e32 v159, v162, v161
	v_fma_f32 v158, -v160, v159, v158
	v_div_fmas_f32 v158, v158, v161, v159
	v_readlane_b32 vcc_lo, v254, 8
	v_div_fixup_f32 v155, v158, v155, s3
	v_readlane_b32 vcc_hi, v254, 9
	v_readlane_b32 s3, v255, 0
	v_mul_f32_e32 v114, v114, v155
	v_lshl_add_u64 v[156:157], vcc, 0, v[156:157]
	s_add_i32 s3, s74, s3
	global_store_dword v[156:157], v114, off
	v_add_u32_e32 v114, s3, v154
	v_add_u32_e32 v154, 0x18308, v114
	v_add_u32_e32 v114, 0x18508, v114
	ds_write_b8 v154, v230
	ds_write_b8 v114, v149
	s_branch .LBB0_584
